# attention Q loads (read once per unit) marked nt to keep the A2 gate columns resident for A6; on top of v040
# speedup vs baseline: 1.0017x; 1.0017x over previous
.LBB0_890:
	s_or_b64 exec, exec, s[20:21]
	s_mul_i32 s12, s19, 0x600
	s_mul_hi_u32 s13, s18, 0x600
	s_add_i32 s13, s13, s12
	s_mul_i32 s12, s18, 0x600
	s_add_u32 s12, s66, s12
	s_addc_u32 s13, s67, s13
	s_add_u32 s10, s12, s10
	s_addc_u32 s11, s13, s11
	s_lshl_b32 s24, s44, 5
	s_mul_i32 s12, s44, 0xc000
	s_mul_hi_i32 s13, s24, 0x600
	s_add_u32 s10, s10, s12
	s_addc_u32 s11, s11, s13
	v_mov_b32_e32 v219, v3
	v_lshl_add_u64 v[4:5], s[10:11], 0, v[218:219]
	v_lshlrev_b32_e32 v2, 1, v210
	v_lshl_add_u64 v[4:5], v[4:5], 0, v[2:3]
	global_load_dwordx4 v[134:137], v[4:5], off nt
	global_load_dwordx4 v[130:133], v[4:5], off offset:32 nt
	global_load_dwordx4 v[126:129], v[4:5], off offset:64 nt
	global_load_dwordx4 v[122:125], v[4:5], off offset:96 nt
	global_load_dwordx4 v[118:121], v[4:5], off offset:128 nt
	global_load_dwordx4 v[114:117], v[4:5], off offset:160 nt
	v_lshl_add_u64 v[4:5], v[234:235], 0, s[80:81]
	s_add_i32 s10, s46, 0x6000
	s_mov_b32 s11, m0
	s_mov_b32 m0, s10
	s_nop 0
	global_load_lds_dwordx4 v[4:5], off
	s_mov_b32 m0, s11
	s_and_saveexec_b64 s[10:11], s[4:5]
	s_cbranch_execz .LBB0_892
	v_lshl_add_u64 v[4:5], v[236:237], 0, s[80:81]
	s_add_i32 s12, s47, 0x6000
	s_mov_b32 s13, m0
	s_mov_b32 m0, s12
	s_nop 0
	global_load_lds_dwordx4 v[4:5], off
	s_mov_b32 m0, s13

.LBB0_907:
	s_and_b64 vcc, exec, s[20:21]
	s_cbranch_vccz .LBB0_916
	s_mul_i32 s10, s19, 0x1c00
	s_mul_hi_u32 s11, s18, 0x1c00
	s_add_i32 s11, s11, s10
	s_mul_i32 s10, s18, 0x1c00
	s_add_u32 s12, s62, s10
	s_addc_u32 s13, s63, s11
	s_lshl_b32 s10, s43, 6
	s_ashr_i32 s11, s10, 31
	s_lshl_b64 s[22:23], s[10:11], 1
	s_add_u32 s24, s12, s22
	s_addc_u32 s25, s13, s23
	s_mul_hi_u32 s10, s42, 0x39c0000
	s_mul_i32 s42, s42, 0x39c0000
	s_add_u32 s12, s62, s42
	s_addc_u32 s13, s63, s10
	s_lshl_b32 s10, s43, 4
	s_andn2_b32 s10, s10, 63
	s_ashr_i32 s11, s10, 31
	s_lshl_b64 s[10:11], s[10:11], 1
	s_add_u32 s12, s12, s10
	v_readfirstlane_b32 s21, v1
	s_addc_u32 s13, s13, s11
	s_ashr_i32 s20, s21, 6
	s_lshl_b32 s10, s20, 5
	s_mul_i32 s11, s20, 0x38000
	s_mul_hi_i32 s26, s10, 0x1c00
	s_add_u32 s24, s24, s11
	s_addc_u32 s25, s25, s26
	s_lshl_b32 s11, s20, 4
	v_and_or_b32 v2, s11, 48, v252
	v_mov_b32_e32 v229, v3
	s_lshl_b32 s26, s20, 3
	v_mul_u32_u24_e32 v2, 0xe00, v2
	v_lshl_add_u64 v[4:5], s[12:13], 0, v[228:229]
	s_ashr_i32 s27, s26, 31
	v_lshlrev_b32_e32 v2, 1, v2
	s_ashr_i32 s11, s21, 3
	v_lshl_add_u64 v[44:45], s[26:27], 1, v[4:5]
	v_lshl_add_u64 v[4:5], s[12:13], 0, v[2:3]
	s_and_b32 s12, s11, 0xffffffe0
	s_ashr_i32 s13, s12, 31
	v_lshl_add_u64 v[4:5], s[12:13], 1, v[4:5]
	v_lshlrev_b32_e32 v2, 1, v214
	s_mov_b64 s[26:27], 0xa00
	v_lshl_add_u64 v[46:47], v[4:5], 0, v[2:3]
	s_mov_b64 s[12:13], 0xb00
	s_lshl_b32 s36, s20, 10
	v_lshl_add_u64 v[164:165], v[44:45], 0, s[26:27]
	v_lshl_add_u64 v[68:69], v[46:47], 0, s[12:13]
	s_add_i32 s36, s36, 0
	s_mov_b32 s11, m0
	s_mov_b32 m0, s36
	s_nop 0
	global_load_lds_dwordx4 v[164:165], off
	s_mov_b32 m0, s11
	s_mov_b64 s[12:13], 0x70a00
	s_add_i32 s38, s36, 0x6000
	s_mov_b32 s11, m0
	s_mov_b32 m0, s38
	s_nop 0
	global_load_lds_dwordx4 v[68:69], off
	s_mov_b32 m0, s11
	v_lshl_add_u64 v[4:5], v[44:45], 0, s[12:13]
	v_mov_b32_e32 v231, v3
	s_add_i32 s11, s36, 0x2000
	s_mov_b32 s12, m0
	s_mov_b32 m0, s11
	s_nop 0
	global_load_lds_dwordx4 v[4:5], off
	s_mov_b32 m0, s12
	v_lshl_add_u64 v[4:5], s[24:25], 0, v[230:231]
	v_lshlrev_b32_e32 v2, 1, v210
	v_lshl_add_u64 v[4:5], v[4:5], 0, v[2:3]
	global_load_dwordx4 v[112:115], v[4:5], off offset:1536 nt
	global_load_dwordx4 v[108:111], v[4:5], off offset:1568 nt
	global_load_dwordx4 v[104:107], v[4:5], off offset:1600 nt
	global_load_dwordx4 v[100:103], v[4:5], off offset:1632 nt
	s_mov_b64 s[12:13], 0xe0a00
	s_add_i32 s11, s36, 0x4000
	v_lshl_add_u64 v[4:5], v[44:45], 0, s[12:13]
	s_mov_b32 s12, m0
	s_mov_b32 m0, s11
	s_nop 0
	global_load_lds_dwordx4 v[4:5], off
	s_mov_b32 m0, s12
	s_waitcnt vmcnt(3) lgkmcnt(0)
	s_barrier
	ds_read_b128 v[4:7], v253
	ds_read_b128 v[20:23], v253 offset:512
	ds_read_b128 v[36:39], v253 offset:2048
	ds_read_b128 v[40:43], v253 offset:2560
	s_mov_b64 s[26:27], 0x150a00
	s_add_i32 s11, s36, 0x8000
	s_mov_b32 s24, 1
	s_movk_i32 s12, 0x2000
	s_movk_i32 s91, 0x4000
	s_mov_b32 s40, 0
	s_andn2_b64 vcc, exec, s[8:9]
	s_waitcnt vmcnt(0) lgkmcnt(0)
	v_mfma_f32_32x32x16_bf16 v[4:19], v[4:7], v[112:115], 0
	v_mfma_f32_32x32x16_bf16 v[20:35], v[20:23], v[112:115], 0
	v_mfma_f32_32x32x16_bf16 v[4:19], v[36:39], v[108:111], v[4:19]
	ds_read_b128 v[36:39], v253 offset:4096
	v_mfma_f32_32x32x16_bf16 v[20:35], v[40:43], v[108:111], v[20:35]
	ds_read_b128 v[40:43], v253 offset:4608
	s_waitcnt lgkmcnt(1)
	v_mfma_f32_32x32x16_bf16 v[4:19], v[36:39], v[104:107], v[4:19]
	ds_read_b128 v[36:39], v253 offset:6144
	s_waitcnt lgkmcnt(1)
	v_mfma_f32_32x32x16_bf16 v[20:35], v[40:43], v[104:107], v[20:35]
	ds_read_b128 v[40:43], v253 offset:6656
	s_waitcnt vmcnt(0) lgkmcnt(0)
	s_barrier
	s_waitcnt lgkmcnt(1)
	v_mfma_f32_32x32x16_bf16 v[4:19], v[36:39], v[100:103], v[4:19]
	v_lshl_add_u64 v[36:37], v[44:45], 0, s[26:27]
	s_mov_b64 s[26:27], 0x70b00
	s_mov_b32 s13, m0
	s_mov_b32 m0, s36
	s_nop 0
	global_load_lds_dwordx4 v[36:37], off
	s_mov_b32 m0, s13
	v_lshl_add_u64 v[166:167], v[46:47], 0, s[26:27]
	s_mov_b32 s13, m0
	s_mov_b32 m0, s11
	s_nop 0
	global_load_lds_dwordx4 v[166:167], off
	s_mov_b32 m0, s13
	ds_read_b128 v[160:163], v253 offset:8192
	ds_read_b128 v[152:155], v253 offset:8704
	ds_read_b128 v[156:159], v253 offset:10240
	ds_read_b128 v[148:151], v253 offset:10752
	ds_read_b128 v[144:147], v253 offset:12288
	ds_read_b128 v[140:143], v253 offset:12800
	ds_read_b128 v[136:139], v253 offset:14336
	ds_read_b128 v[132:135], v253 offset:14848
	s_waitcnt vmcnt(2) lgkmcnt(0)
	s_barrier
	s_waitcnt lgkmcnt(8)
	v_mfma_f32_32x32x16_bf16 v[20:35], v[40:43], v[100:103], v[20:35]
	v_exp_f32_e32 v52, v4
	v_exp_f32_e32 v53, v5
	v_exp_f32_e32 v54, v6
	v_exp_f32_e32 v55, v7
	v_exp_f32_e32 v56, v8
	v_exp_f32_e32 v57, v9
	v_exp_f32_e32 v58, v10
	v_exp_f32_e32 v59, v11
	v_exp_f32_e32 v60, v12
	v_exp_f32_e32 v61, v13
	v_exp_f32_e32 v62, v14
	v_exp_f32_e32 v63, v15
	v_exp_f32_e32 v64, v16
	v_exp_f32_e32 v65, v17
	v_exp_f32_e32 v66, v18
	v_exp_f32_e32 v67, v19
	v_exp_f32_e32 v36, v20
	v_exp_f32_e32 v37, v21
	v_exp_f32_e32 v38, v22
	v_exp_f32_e32 v39, v23
	v_exp_f32_e32 v40, v24
	v_exp_f32_e32 v41, v25
	v_exp_f32_e32 v42, v26
	v_exp_f32_e32 v43, v27
	v_exp_f32_e32 v44, v28
	v_exp_f32_e32 v45, v29
	v_exp_f32_e32 v46, v30
	v_exp_f32_e32 v47, v31
	v_exp_f32_e32 v48, v32
	v_exp_f32_e32 v49, v33
	v_exp_f32_e32 v50, v34
	v_exp_f32_e32 v51, v35
	s_cbranch_vccnz .LBB0_961
	s_mov_b64 s[8:9], 0x150000
	v_lshl_add_u64 v[168:169], v[68:69], 0, s[8:9]
	s_mov_b64 s[8:9], 0x230000
	v_mov_b32_e32 v176, 0
	v_lshl_add_u64 v[170:171], v[164:165], 0, s[8:9]
	s_mov_b32 s11, 0
	s_mov_b32 s24, 6
	s_movk_i32 s39, 0x2000
	s_movk_i32 s13, 0x4000
	v_mov_b32_e32 v4, 0
	v_mov_b32_e32 v5, v176
	v_mov_b32_e32 v6, v176
	v_mov_b32_e32 v7, v176
	v_mov_b32_e32 v8, v176
	v_mov_b32_e32 v9, v176
	v_mov_b32_e32 v10, v176
	v_mov_b32_e32 v11, v176
	v_mov_b32_e32 v12, v176
	v_mov_b32_e32 v13, v176
	v_mov_b32_e32 v14, v176
	v_mov_b32_e32 v15, v176
	v_mov_b32_e32 v16, v176
	v_mov_b32_e32 v17, v176
	v_mov_b32_e32 v18, v176
	v_mov_b32_e32 v19, v176
	v_mov_b32_e32 v20, 0
	v_mov_b32_e32 v21, v176
	v_mov_b32_e32 v22, v176
	v_mov_b32_e32 v23, v176
	v_mov_b32_e32 v24, v176
	v_mov_b32_e32 v25, v176
	v_mov_b32_e32 v26, v176
	v_mov_b32_e32 v27, v176
	v_mov_b32_e32 v28, v176
	v_mov_b32_e32 v29, v176
	v_mov_b32_e32 v30, v176
	v_mov_b32_e32 v31, v176
	v_mov_b32_e32 v32, v176
	v_mov_b32_e32 v33, v176
	v_mov_b32_e32 v34, v176
	v_mov_b32_e32 v35, v176
